# v43 + lever 7 instruction selection: attention fast-path row sums with v_pk_add_f32 (15 scalar adds -> 7 packed + 1 per half)
# baseline (speedup 1.0000x reference)
.LBB0_556:
	s_cmp_le_i32 s63, s28
	s_cbranch_scc0 .Lorig_a0b0
	s_cmp_eq_u32 s17, 0
	s_cbranch_scc1 .Lorig_a0b0
	s_setprio 3
	ds_read_b128 v[116:119], v189 offset:0
	ds_read_b128 v[120:123], v226 offset:0
	ds_read_b128 v[124:127], v227 offset:0
	ds_read_b128 v[128:131], v228 offset:0
	s_waitcnt lgkmcnt(3)
	v_mfma_f32_32x32x16_bf16 v[84:99], v[116:119], v[132:135], 0
	ds_read_b128 v[116:119], v232 offset:0
	s_waitcnt lgkmcnt(3)
	v_mfma_f32_32x32x16_bf16 v[84:99], v[120:123], v[136:139], v[84:99]
	ds_read_b128 v[120:123], v233 offset:0
	s_waitcnt lgkmcnt(3)
	v_mfma_f32_32x32x16_bf16 v[84:99], v[124:127], v[140:143], v[84:99]
	ds_read_b128 v[124:127], v234 offset:0
	s_waitcnt lgkmcnt(3)
	v_mfma_f32_32x32x16_bf16 v[84:99], v[128:131], v[144:147], v[84:99]
	ds_read_b128 v[128:131], v235 offset:0
	s_waitcnt lgkmcnt(3)
	v_mfma_f32_32x32x16_bf16 v[84:99], v[116:119], v[148:151], v[84:99]
	ds_read_b128 v[116:119], v190 offset:0
	s_waitcnt lgkmcnt(3)
	v_mfma_f32_32x32x16_bf16 v[84:99], v[120:123], v[152:155], v[84:99]
	ds_read_b128 v[120:123], v229 offset:0
	s_waitcnt lgkmcnt(3)
	v_mfma_f32_32x32x16_bf16 v[84:99], v[124:127], v[156:159], v[84:99]
	ds_read_b128 v[124:127], v230 offset:0
	s_waitcnt lgkmcnt(3)
	v_mfma_f32_32x32x16_bf16 v[84:99], v[128:131], v[160:163], v[84:99]
	ds_read_b128 v[128:131], v231 offset:0
	s_waitcnt lgkmcnt(3)
	v_mfma_f32_32x32x16_bf16 v[84:99], v[116:119], v[164:167], v[84:99]
	ds_read_b128 v[116:119], v189 offset:8192
	s_waitcnt lgkmcnt(3)
	v_mfma_f32_32x32x16_bf16 v[84:99], v[120:123], v[172:175], v[84:99]
	ds_read_b128 v[120:123], v226 offset:8192
	s_waitcnt lgkmcnt(3)
	v_mfma_f32_32x32x16_bf16 v[84:99], v[124:127], v[168:171], v[84:99]
	ds_read_b128 v[124:127], v227 offset:8192
	s_waitcnt lgkmcnt(3)
	v_mfma_f32_32x32x16_bf16 v[84:99], v[128:131], v[176:179], v[84:99]
	ds_read_b128 v[128:131], v228 offset:8192
	s_waitcnt lgkmcnt(3)
	v_mfma_f32_32x32x16_bf16 v[68:83], v[116:119], v[132:135], 0
	ds_read_b128 v[116:119], v232 offset:8192
	s_waitcnt lgkmcnt(3)
	v_mfma_f32_32x32x16_bf16 v[68:83], v[120:123], v[136:139], v[68:83]
	ds_read_b128 v[120:123], v233 offset:8192
	s_waitcnt lgkmcnt(3)
	v_mfma_f32_32x32x16_bf16 v[68:83], v[124:127], v[140:143], v[68:83]
	ds_read_b128 v[124:127], v234 offset:8192
	s_waitcnt lgkmcnt(3)
	v_mfma_f32_32x32x16_bf16 v[68:83], v[128:131], v[144:147], v[68:83]
	ds_read_b128 v[128:131], v235 offset:8192
	s_waitcnt lgkmcnt(3)
	v_mfma_f32_32x32x16_bf16 v[68:83], v[116:119], v[148:151], v[68:83]
	ds_read_b128 v[116:119], v190 offset:4096
	s_waitcnt lgkmcnt(3)
	v_mfma_f32_32x32x16_bf16 v[68:83], v[120:123], v[152:155], v[68:83]
	ds_read_b128 v[120:123], v229 offset:4096
	s_waitcnt lgkmcnt(3)
	v_mfma_f32_32x32x16_bf16 v[68:83], v[124:127], v[156:159], v[68:83]
	ds_read_b128 v[124:127], v230 offset:4096
	s_waitcnt lgkmcnt(3)
	v_mfma_f32_32x32x16_bf16 v[68:83], v[128:131], v[160:163], v[68:83]
	ds_read_b128 v[128:131], v231 offset:4096
	s_waitcnt lgkmcnt(3)
	v_mfma_f32_32x32x16_bf16 v[68:83], v[116:119], v[164:167], v[68:83]
	s_waitcnt lgkmcnt(2)
	v_mfma_f32_32x32x16_bf16 v[68:83], v[120:123], v[172:175], v[68:83]
	s_waitcnt lgkmcnt(1)
	v_mfma_f32_32x32x16_bf16 v[68:83], v[124:127], v[168:171], v[68:83]
	s_waitcnt lgkmcnt(0)
	v_mfma_f32_32x32x16_bf16 v[68:83], v[128:131], v[176:179], v[68:83]
	ds_read_b64_tr_b16 v[116:117], v191 offset:0
	ds_read_b64_tr_b16 v[118:119], v191 offset:2048
	ds_read_b64_tr_b16 v[120:121], v191 offset:4096
	ds_read_b64_tr_b16 v[122:123], v191 offset:6144
	ds_read_b64_tr_b16 v[124:125], v191 offset:8192
	ds_read_b64_tr_b16 v[126:127], v191 offset:10240
	ds_read_b64_tr_b16 v[128:129], v191 offset:12288
	ds_read_b64_tr_b16 v[130:131], v191 offset:14336
	s_setprio 0
	s_nop 7
	s_nop 3
	v_cmp_eq_f32_e32 vcc, 0, v223
	s_cmp_eq_u64 vcc, exec
	s_cbranch_scc0 .Lsub_a0b0
	v_exp_f32_e32 v100, v84
	v_exp_f32_e32 v101, v85
	v_exp_f32_e32 v102, v86
	v_exp_f32_e32 v103, v87
	v_exp_f32_e32 v104, v88
	v_exp_f32_e32 v105, v89
	v_exp_f32_e32 v106, v90
	v_exp_f32_e32 v107, v91
	v_exp_f32_e32 v108, v92
	v_exp_f32_e32 v109, v93
	v_exp_f32_e32 v110, v94
	v_exp_f32_e32 v111, v95
	v_exp_f32_e32 v112, v96
	v_exp_f32_e32 v113, v97
	v_exp_f32_e32 v114, v98
	v_exp_f32_e32 v115, v99
	v_pk_add_f32 v[250:251], v[100:101], v[102:103]
	v_pk_add_f32 v[250:251], v[250:251], v[104:105]
	v_pk_add_f32 v[250:251], v[250:251], v[106:107]
	v_pk_add_f32 v[250:251], v[250:251], v[108:109]
	v_pk_add_f32 v[250:251], v[250:251], v[110:111]
	v_pk_add_f32 v[250:251], v[250:251], v[112:113]
	v_pk_add_f32 v[250:251], v[250:251], v[114:115]
	v_add_f32_e32 v237, v250, v251
	v_cvt_pk_bf16_f32 v238, v100, v101
	v_cvt_pk_bf16_f32 v239, v102, v103
	v_cvt_pk_bf16_f32 v240, v104, v105
	v_cvt_pk_bf16_f32 v241, v106, v107
	v_cvt_pk_bf16_f32 v242, v108, v109
	v_cvt_pk_bf16_f32 v243, v110, v111
	v_cvt_pk_bf16_f32 v244, v112, v113
	v_cvt_pk_bf16_f32 v245, v114, v115
	s_nop 1
	v_permlane32_swap_b32_e32 v238, v240
	v_permlane32_swap_b32_e32 v239, v241
	v_permlane32_swap_b32_e32 v242, v244
	v_permlane32_swap_b32_e32 v243, v245
	v_exp_f32_e32 v100, v68
	v_exp_f32_e32 v101, v69
	v_exp_f32_e32 v102, v70
	v_exp_f32_e32 v103, v71
	v_exp_f32_e32 v104, v72
	v_exp_f32_e32 v105, v73
	v_exp_f32_e32 v106, v74
	v_exp_f32_e32 v107, v75
	v_exp_f32_e32 v108, v76
	v_exp_f32_e32 v109, v77
	v_exp_f32_e32 v110, v78
	v_exp_f32_e32 v111, v79
	v_exp_f32_e32 v112, v80
	v_exp_f32_e32 v113, v81
	v_exp_f32_e32 v114, v82
	v_exp_f32_e32 v115, v83
	v_pk_add_f32 v[250:251], v[100:101], v[102:103]
	v_pk_add_f32 v[250:251], v[250:251], v[104:105]
	v_pk_add_f32 v[250:251], v[250:251], v[106:107]
	v_pk_add_f32 v[250:251], v[250:251], v[108:109]
	v_pk_add_f32 v[250:251], v[250:251], v[110:111]
	v_pk_add_f32 v[250:251], v[250:251], v[112:113]
	v_pk_add_f32 v[250:251], v[250:251], v[114:115]
	v_add_f32_e32 v250, v250, v251
	v_cvt_pk_bf16_f32 v100, v100, v101
	v_cvt_pk_bf16_f32 v101, v102, v103
	v_cvt_pk_bf16_f32 v102, v104, v105
	v_cvt_pk_bf16_f32 v103, v106, v107
	v_cvt_pk_bf16_f32 v104, v108, v109
	v_cvt_pk_bf16_f32 v105, v110, v111
	v_cvt_pk_bf16_f32 v106, v112, v113
	v_cvt_pk_bf16_f32 v107, v114, v115
	s_nop 1
	v_permlane32_swap_b32_e32 v100, v102
	v_permlane32_swap_b32_e32 v101, v103
	v_permlane32_swap_b32_e32 v104, v106
	v_permlane32_swap_b32_e32 v105, v107
	s_branch .Lsum_a0b0
.Lsub_a0b0:
	v_sub_f32_e32 v100, v84, v223
	v_sub_f32_e32 v101, v85, v223
	v_sub_f32_e32 v102, v86, v223
	v_sub_f32_e32 v103, v87, v223
	v_sub_f32_e32 v104, v88, v223
	v_sub_f32_e32 v105, v89, v223
	v_sub_f32_e32 v106, v90, v223
	v_sub_f32_e32 v107, v91, v223
	v_sub_f32_e32 v108, v92, v223
	v_sub_f32_e32 v109, v93, v223
	v_sub_f32_e32 v110, v94, v223
	v_sub_f32_e32 v111, v95, v223
	v_sub_f32_e32 v112, v96, v223
	v_sub_f32_e32 v113, v97, v223
	v_sub_f32_e32 v114, v98, v223
	v_sub_f32_e32 v115, v99, v223
	v_exp_f32_e32 v100, v100
	v_exp_f32_e32 v101, v101
	v_exp_f32_e32 v102, v102
	v_exp_f32_e32 v103, v103
	v_exp_f32_e32 v104, v104
	v_exp_f32_e32 v105, v105
	v_exp_f32_e32 v106, v106
	v_exp_f32_e32 v107, v107
	v_exp_f32_e32 v108, v108
	v_exp_f32_e32 v109, v109
	v_exp_f32_e32 v110, v110
	v_exp_f32_e32 v111, v111
	v_exp_f32_e32 v112, v112
	v_exp_f32_e32 v113, v113
	v_exp_f32_e32 v114, v114
	v_exp_f32_e32 v115, v115
	v_pk_add_f32 v[250:251], v[100:101], v[102:103]
	v_pk_add_f32 v[250:251], v[250:251], v[104:105]
	v_pk_add_f32 v[250:251], v[250:251], v[106:107]
	v_pk_add_f32 v[250:251], v[250:251], v[108:109]
	v_pk_add_f32 v[250:251], v[250:251], v[110:111]
	v_pk_add_f32 v[250:251], v[250:251], v[112:113]
	v_pk_add_f32 v[250:251], v[250:251], v[114:115]
	v_add_f32_e32 v237, v250, v251
	v_cvt_pk_bf16_f32 v238, v100, v101
	v_cvt_pk_bf16_f32 v239, v102, v103
	v_cvt_pk_bf16_f32 v240, v104, v105
	v_cvt_pk_bf16_f32 v241, v106, v107
	v_cvt_pk_bf16_f32 v242, v108, v109
	v_cvt_pk_bf16_f32 v243, v110, v111
	v_cvt_pk_bf16_f32 v244, v112, v113
	v_cvt_pk_bf16_f32 v245, v114, v115
	s_nop 1
	v_permlane32_swap_b32_e32 v238, v240
	v_permlane32_swap_b32_e32 v239, v241
	v_permlane32_swap_b32_e32 v242, v244
	v_permlane32_swap_b32_e32 v243, v245
	v_sub_f32_e32 v100, v68, v223
	v_sub_f32_e32 v101, v69, v223
	v_sub_f32_e32 v102, v70, v223
	v_sub_f32_e32 v103, v71, v223
	v_sub_f32_e32 v104, v72, v223
	v_sub_f32_e32 v105, v73, v223
	v_sub_f32_e32 v106, v74, v223
	v_sub_f32_e32 v107, v75, v223
	v_sub_f32_e32 v108, v76, v223
	v_sub_f32_e32 v109, v77, v223
	v_sub_f32_e32 v110, v78, v223
	v_sub_f32_e32 v111, v79, v223
	v_sub_f32_e32 v112, v80, v223
	v_sub_f32_e32 v113, v81, v223
	v_sub_f32_e32 v114, v82, v223
	v_sub_f32_e32 v115, v83, v223
	v_exp_f32_e32 v100, v100
	v_exp_f32_e32 v101, v101
	v_exp_f32_e32 v102, v102
	v_exp_f32_e32 v103, v103
	v_exp_f32_e32 v104, v104
	v_exp_f32_e32 v105, v105
	v_exp_f32_e32 v106, v106
	v_exp_f32_e32 v107, v107
	v_exp_f32_e32 v108, v108
	v_exp_f32_e32 v109, v109
	v_exp_f32_e32 v110, v110
	v_exp_f32_e32 v111, v111
	v_exp_f32_e32 v112, v112
	v_exp_f32_e32 v113, v113
	v_exp_f32_e32 v114, v114
	v_exp_f32_e32 v115, v115
	v_pk_add_f32 v[250:251], v[100:101], v[102:103]
	v_pk_add_f32 v[250:251], v[250:251], v[104:105]
	v_pk_add_f32 v[250:251], v[250:251], v[106:107]
	v_pk_add_f32 v[250:251], v[250:251], v[108:109]
	v_pk_add_f32 v[250:251], v[250:251], v[110:111]
	v_pk_add_f32 v[250:251], v[250:251], v[112:113]
	v_pk_add_f32 v[250:251], v[250:251], v[114:115]
	v_add_f32_e32 v250, v250, v251
	v_cvt_pk_bf16_f32 v100, v100, v101
	v_cvt_pk_bf16_f32 v101, v102, v103
	v_cvt_pk_bf16_f32 v102, v104, v105
	v_cvt_pk_bf16_f32 v103, v106, v107
	v_cvt_pk_bf16_f32 v104, v108, v109
	v_cvt_pk_bf16_f32 v105, v110, v111
	v_cvt_pk_bf16_f32 v106, v112, v113
	v_cvt_pk_bf16_f32 v107, v114, v115
	s_nop 1
	v_permlane32_swap_b32_e32 v100, v102
	v_permlane32_swap_b32_e32 v101, v103
	v_permlane32_swap_b32_e32 v104, v106
	v_permlane32_swap_b32_e32 v105, v107

.LBB0_571:
	s_add_i32 s98, s63, 64
	s_cmp_le_i32 s98, s28
	s_cbranch_scc0 .Lorig_a0b1
	s_setprio 3
	ds_read_b128 v[116:119], v189 offset:24576
	ds_read_b128 v[120:123], v226 offset:24576
	ds_read_b128 v[124:127], v227 offset:24576
	ds_read_b128 v[128:131], v228 offset:24576
	s_waitcnt lgkmcnt(3)
	v_mfma_f32_32x32x16_bf16 v[84:99], v[116:119], v[132:135], 0
	ds_read_b128 v[116:119], v232 offset:24576
	s_waitcnt lgkmcnt(3)
	v_mfma_f32_32x32x16_bf16 v[84:99], v[120:123], v[136:139], v[84:99]
	ds_read_b128 v[120:123], v233 offset:24576
	s_waitcnt lgkmcnt(3)
	v_mfma_f32_32x32x16_bf16 v[84:99], v[124:127], v[140:143], v[84:99]
	ds_read_b128 v[124:127], v234 offset:24576
	s_waitcnt lgkmcnt(3)
	v_mfma_f32_32x32x16_bf16 v[84:99], v[128:131], v[144:147], v[84:99]
	ds_read_b128 v[128:131], v235 offset:24576
	s_waitcnt lgkmcnt(3)
	v_mfma_f32_32x32x16_bf16 v[84:99], v[116:119], v[148:151], v[84:99]
	ds_read_b128 v[116:119], v190 offset:24576
	s_waitcnt lgkmcnt(3)
	v_mfma_f32_32x32x16_bf16 v[84:99], v[120:123], v[152:155], v[84:99]
	ds_read_b128 v[120:123], v229 offset:24576
	s_waitcnt lgkmcnt(3)
	v_mfma_f32_32x32x16_bf16 v[84:99], v[124:127], v[156:159], v[84:99]
	ds_read_b128 v[124:127], v230 offset:24576
	s_waitcnt lgkmcnt(3)
	v_mfma_f32_32x32x16_bf16 v[84:99], v[128:131], v[160:163], v[84:99]
	ds_read_b128 v[128:131], v231 offset:24576
	s_waitcnt lgkmcnt(3)
	v_mfma_f32_32x32x16_bf16 v[84:99], v[116:119], v[164:167], v[84:99]
	ds_read_b128 v[116:119], v189 offset:32768
	s_waitcnt lgkmcnt(3)
	v_mfma_f32_32x32x16_bf16 v[84:99], v[120:123], v[172:175], v[84:99]
	ds_read_b128 v[120:123], v226 offset:32768
	s_waitcnt lgkmcnt(3)
	v_mfma_f32_32x32x16_bf16 v[84:99], v[124:127], v[168:171], v[84:99]
	ds_read_b128 v[124:127], v227 offset:32768
	s_waitcnt lgkmcnt(3)
	v_mfma_f32_32x32x16_bf16 v[84:99], v[128:131], v[176:179], v[84:99]
	ds_read_b128 v[128:131], v228 offset:32768
	s_waitcnt lgkmcnt(3)
	v_mfma_f32_32x32x16_bf16 v[68:83], v[116:119], v[132:135], 0
	ds_read_b128 v[116:119], v232 offset:32768
	s_waitcnt lgkmcnt(3)
	v_mfma_f32_32x32x16_bf16 v[68:83], v[120:123], v[136:139], v[68:83]
	ds_read_b128 v[120:123], v233 offset:32768
	s_waitcnt lgkmcnt(3)
	v_mfma_f32_32x32x16_bf16 v[68:83], v[124:127], v[140:143], v[68:83]
	ds_read_b128 v[124:127], v234 offset:32768
	s_waitcnt lgkmcnt(3)
	v_mfma_f32_32x32x16_bf16 v[68:83], v[128:131], v[144:147], v[68:83]
	ds_read_b128 v[128:131], v235 offset:32768
	s_waitcnt lgkmcnt(3)
	v_mfma_f32_32x32x16_bf16 v[68:83], v[116:119], v[148:151], v[68:83]
	ds_read_b128 v[116:119], v190 offset:28672
	s_waitcnt lgkmcnt(3)
	v_mfma_f32_32x32x16_bf16 v[68:83], v[120:123], v[152:155], v[68:83]
	ds_read_b128 v[120:123], v229 offset:28672
	s_waitcnt lgkmcnt(3)
	v_mfma_f32_32x32x16_bf16 v[68:83], v[124:127], v[156:159], v[68:83]
	ds_read_b128 v[124:127], v230 offset:28672
	s_waitcnt lgkmcnt(3)
	v_mfma_f32_32x32x16_bf16 v[68:83], v[128:131], v[160:163], v[68:83]
	ds_read_b128 v[128:131], v231 offset:28672
	s_waitcnt lgkmcnt(3)
	v_mfma_f32_32x32x16_bf16 v[68:83], v[116:119], v[164:167], v[68:83]
	s_waitcnt lgkmcnt(2)
	v_mfma_f32_32x32x16_bf16 v[68:83], v[120:123], v[172:175], v[68:83]
	s_waitcnt lgkmcnt(1)
	v_mfma_f32_32x32x16_bf16 v[68:83], v[124:127], v[168:171], v[68:83]
	s_waitcnt lgkmcnt(0)
	v_mfma_f32_32x32x16_bf16 v[68:83], v[128:131], v[176:179], v[68:83]
	ds_read_b64_tr_b16 v[116:117], v191 offset:16384
	ds_read_b64_tr_b16 v[118:119], v191 offset:18432
	ds_read_b64_tr_b16 v[120:121], v191 offset:20480
	ds_read_b64_tr_b16 v[122:123], v191 offset:22528
	ds_read_b64_tr_b16 v[124:125], v191 offset:24576
	ds_read_b64_tr_b16 v[126:127], v191 offset:26624
	ds_read_b64_tr_b16 v[128:129], v191 offset:28672
	ds_read_b64_tr_b16 v[130:131], v191 offset:30720
	s_setprio 0
	s_nop 7
	s_nop 3
	v_cmp_eq_f32_e32 vcc, 0, v222
	s_cmp_eq_u64 vcc, exec
	s_cbranch_scc0 .Lsub_a0b1
	v_exp_f32_e32 v100, v84
	v_exp_f32_e32 v101, v85
	v_exp_f32_e32 v102, v86
	v_exp_f32_e32 v103, v87
	v_exp_f32_e32 v104, v88
	v_exp_f32_e32 v105, v89
	v_exp_f32_e32 v106, v90
	v_exp_f32_e32 v107, v91
	v_exp_f32_e32 v108, v92
	v_exp_f32_e32 v109, v93
	v_exp_f32_e32 v110, v94
	v_exp_f32_e32 v111, v95
	v_exp_f32_e32 v112, v96
	v_exp_f32_e32 v113, v97
	v_exp_f32_e32 v114, v98
	v_exp_f32_e32 v115, v99
	v_pk_add_f32 v[250:251], v[100:101], v[102:103]
	v_pk_add_f32 v[250:251], v[250:251], v[104:105]
	v_pk_add_f32 v[250:251], v[250:251], v[106:107]
	v_pk_add_f32 v[250:251], v[250:251], v[108:109]
	v_pk_add_f32 v[250:251], v[250:251], v[110:111]
	v_pk_add_f32 v[250:251], v[250:251], v[112:113]
	v_pk_add_f32 v[250:251], v[250:251], v[114:115]
	v_add_f32_e32 v237, v250, v251
	v_cvt_pk_bf16_f32 v238, v100, v101
	v_cvt_pk_bf16_f32 v239, v102, v103
	v_cvt_pk_bf16_f32 v240, v104, v105
	v_cvt_pk_bf16_f32 v241, v106, v107
	v_cvt_pk_bf16_f32 v242, v108, v109
	v_cvt_pk_bf16_f32 v243, v110, v111
	v_cvt_pk_bf16_f32 v244, v112, v113
	v_cvt_pk_bf16_f32 v245, v114, v115
	s_nop 1
	v_permlane32_swap_b32_e32 v238, v240
	v_permlane32_swap_b32_e32 v239, v241
	v_permlane32_swap_b32_e32 v242, v244
	v_permlane32_swap_b32_e32 v243, v245
	v_exp_f32_e32 v100, v68
	v_exp_f32_e32 v101, v69
	v_exp_f32_e32 v102, v70
	v_exp_f32_e32 v103, v71
	v_exp_f32_e32 v104, v72
	v_exp_f32_e32 v105, v73
	v_exp_f32_e32 v106, v74
	v_exp_f32_e32 v107, v75
	v_exp_f32_e32 v108, v76
	v_exp_f32_e32 v109, v77
	v_exp_f32_e32 v110, v78
	v_exp_f32_e32 v111, v79
	v_exp_f32_e32 v112, v80
	v_exp_f32_e32 v113, v81
	v_exp_f32_e32 v114, v82
	v_exp_f32_e32 v115, v83
	v_pk_add_f32 v[250:251], v[100:101], v[102:103]
	v_pk_add_f32 v[250:251], v[250:251], v[104:105]
	v_pk_add_f32 v[250:251], v[250:251], v[106:107]
	v_pk_add_f32 v[250:251], v[250:251], v[108:109]
	v_pk_add_f32 v[250:251], v[250:251], v[110:111]
	v_pk_add_f32 v[250:251], v[250:251], v[112:113]
	v_pk_add_f32 v[250:251], v[250:251], v[114:115]
	v_add_f32_e32 v250, v250, v251
	v_cvt_pk_bf16_f32 v100, v100, v101
	v_cvt_pk_bf16_f32 v101, v102, v103
	v_cvt_pk_bf16_f32 v102, v104, v105
	v_cvt_pk_bf16_f32 v103, v106, v107
	v_cvt_pk_bf16_f32 v104, v108, v109
	v_cvt_pk_bf16_f32 v105, v110, v111
	v_cvt_pk_bf16_f32 v106, v112, v113
	v_cvt_pk_bf16_f32 v107, v114, v115
	s_nop 1
	v_permlane32_swap_b32_e32 v100, v102
	v_permlane32_swap_b32_e32 v101, v103
	v_permlane32_swap_b32_e32 v104, v106
	v_permlane32_swap_b32_e32 v105, v107
	s_branch .Lsum_a0b1
.Lsub_a0b1:
	v_sub_f32_e32 v100, v84, v222
	v_sub_f32_e32 v101, v85, v222
	v_sub_f32_e32 v102, v86, v222
	v_sub_f32_e32 v103, v87, v222
	v_sub_f32_e32 v104, v88, v222
	v_sub_f32_e32 v105, v89, v222
	v_sub_f32_e32 v106, v90, v222
	v_sub_f32_e32 v107, v91, v222
	v_sub_f32_e32 v108, v92, v222
	v_sub_f32_e32 v109, v93, v222
	v_sub_f32_e32 v110, v94, v222
	v_sub_f32_e32 v111, v95, v222
	v_sub_f32_e32 v112, v96, v222
	v_sub_f32_e32 v113, v97, v222
	v_sub_f32_e32 v114, v98, v222
	v_sub_f32_e32 v115, v99, v222
	v_exp_f32_e32 v100, v100
	v_exp_f32_e32 v101, v101
	v_exp_f32_e32 v102, v102
	v_exp_f32_e32 v103, v103
	v_exp_f32_e32 v104, v104
	v_exp_f32_e32 v105, v105
	v_exp_f32_e32 v106, v106
	v_exp_f32_e32 v107, v107
	v_exp_f32_e32 v108, v108
	v_exp_f32_e32 v109, v109
	v_exp_f32_e32 v110, v110
	v_exp_f32_e32 v111, v111
	v_exp_f32_e32 v112, v112
	v_exp_f32_e32 v113, v113
	v_exp_f32_e32 v114, v114
	v_exp_f32_e32 v115, v115
	v_pk_add_f32 v[250:251], v[100:101], v[102:103]
	v_pk_add_f32 v[250:251], v[250:251], v[104:105]
	v_pk_add_f32 v[250:251], v[250:251], v[106:107]
	v_pk_add_f32 v[250:251], v[250:251], v[108:109]
	v_pk_add_f32 v[250:251], v[250:251], v[110:111]
	v_pk_add_f32 v[250:251], v[250:251], v[112:113]
	v_pk_add_f32 v[250:251], v[250:251], v[114:115]
	v_add_f32_e32 v237, v250, v251
	v_cvt_pk_bf16_f32 v238, v100, v101
	v_cvt_pk_bf16_f32 v239, v102, v103
	v_cvt_pk_bf16_f32 v240, v104, v105
	v_cvt_pk_bf16_f32 v241, v106, v107
	v_cvt_pk_bf16_f32 v242, v108, v109
	v_cvt_pk_bf16_f32 v243, v110, v111
	v_cvt_pk_bf16_f32 v244, v112, v113
	v_cvt_pk_bf16_f32 v245, v114, v115
	s_nop 1
	v_permlane32_swap_b32_e32 v238, v240
	v_permlane32_swap_b32_e32 v239, v241
	v_permlane32_swap_b32_e32 v242, v244
	v_permlane32_swap_b32_e32 v243, v245
	v_sub_f32_e32 v100, v68, v222
	v_sub_f32_e32 v101, v69, v222
	v_sub_f32_e32 v102, v70, v222
	v_sub_f32_e32 v103, v71, v222
	v_sub_f32_e32 v104, v72, v222
	v_sub_f32_e32 v105, v73, v222
	v_sub_f32_e32 v106, v74, v222
	v_sub_f32_e32 v107, v75, v222
	v_sub_f32_e32 v108, v76, v222
	v_sub_f32_e32 v109, v77, v222
	v_sub_f32_e32 v110, v78, v222
	v_sub_f32_e32 v111, v79, v222
	v_sub_f32_e32 v112, v80, v222
	v_sub_f32_e32 v113, v81, v222
	v_sub_f32_e32 v114, v82, v222
	v_sub_f32_e32 v115, v83, v222
	v_exp_f32_e32 v100, v100
	v_exp_f32_e32 v101, v101
	v_exp_f32_e32 v102, v102
	v_exp_f32_e32 v103, v103
	v_exp_f32_e32 v104, v104
	v_exp_f32_e32 v105, v105
	v_exp_f32_e32 v106, v106
	v_exp_f32_e32 v107, v107
	v_exp_f32_e32 v108, v108
	v_exp_f32_e32 v109, v109
	v_exp_f32_e32 v110, v110
	v_exp_f32_e32 v111, v111
	v_exp_f32_e32 v112, v112
	v_exp_f32_e32 v113, v113
	v_exp_f32_e32 v114, v114
	v_exp_f32_e32 v115, v115
	v_pk_add_f32 v[250:251], v[100:101], v[102:103]
	v_pk_add_f32 v[250:251], v[250:251], v[104:105]
	v_pk_add_f32 v[250:251], v[250:251], v[106:107]
	v_pk_add_f32 v[250:251], v[250:251], v[108:109]
	v_pk_add_f32 v[250:251], v[250:251], v[110:111]
	v_pk_add_f32 v[250:251], v[250:251], v[112:113]
	v_pk_add_f32 v[250:251], v[250:251], v[114:115]
	v_add_f32_e32 v250, v250, v251
	v_cvt_pk_bf16_f32 v100, v100, v101
	v_cvt_pk_bf16_f32 v101, v102, v103
	v_cvt_pk_bf16_f32 v102, v104, v105
	v_cvt_pk_bf16_f32 v103, v106, v107
	v_cvt_pk_bf16_f32 v104, v108, v109
	v_cvt_pk_bf16_f32 v105, v110, v111
	v_cvt_pk_bf16_f32 v106, v112, v113
	v_cvt_pk_bf16_f32 v107, v114, v115
	s_nop 1
	v_permlane32_swap_b32_e32 v100, v102
	v_permlane32_swap_b32_e32 v101, v103
	v_permlane32_swap_b32_e32 v104, v106
	v_permlane32_swap_b32_e32 v105, v107

.LBB0_1452:
	s_cmp_le_i32 s18, s40
	s_cbranch_scc0 .Lorig_a1b0
	s_cmp_eq_u32 s71, 0
	s_cbranch_scc1 .Lorig_a1b0
	s_setprio 3
	ds_read_b128 v[140:143], v176
	ds_read_b128 v[144:147], v176 offset:32
	ds_read_b128 v[148:151], v176 offset:64
	ds_read_b128 v[152:155], v176 offset:96
	ds_read_b128 v[208:211], v172 offset:32768
	ds_read_b128 v[212:215], v206 offset:32768
	ds_read_b128 v[216:219], v207 offset:32768
	ds_read_b128 v[220:223], v237 offset:32768
	ds_read_b128 v[224:227], v244 offset:32768
	ds_read_b128 v[228:231], v245 offset:32768
	ds_read_b128 v[232:235], v246 offset:32768
	ds_read_b128 v[238:241], v247 offset:32768
	ds_read_b128 v[156:159], v176 offset:128
	ds_read_b128 v[160:163], v176 offset:160
	ds_read_b128 v[164:167], v176 offset:192
	ds_read_b128 v[168:171], v176 offset:224
	s_waitcnt lgkmcnt(11)
	v_mfma_f32_32x32x16_bf16 v[84:99], v[208:211], v[100:103], v[140:155]
	ds_read_b128 v[208:211], v172 offset:40960
	s_waitcnt lgkmcnt(11)
	v_mfma_f32_32x32x16_bf16 v[84:99], v[212:215], v[104:107], v[84:99]
	ds_read_b128 v[212:215], v206 offset:40960
	s_waitcnt lgkmcnt(11)
	v_mfma_f32_32x32x16_bf16 v[84:99], v[216:219], v[108:111], v[84:99]
	ds_read_b128 v[216:219], v207 offset:40960
	s_waitcnt lgkmcnt(11)
	v_mfma_f32_32x32x16_bf16 v[84:99], v[220:223], v[112:115], v[84:99]
	ds_read_b128 v[220:223], v237 offset:40960
	s_waitcnt lgkmcnt(11)
	v_mfma_f32_32x32x16_bf16 v[84:99], v[224:227], v[116:119], v[84:99]
	ds_read_b128 v[224:227], v244 offset:40960
	s_waitcnt lgkmcnt(11)
	v_mfma_f32_32x32x16_bf16 v[84:99], v[228:231], v[120:123], v[84:99]
	ds_read_b128 v[228:231], v245 offset:40960
	s_waitcnt lgkmcnt(11)
	v_mfma_f32_32x32x16_bf16 v[84:99], v[232:235], v[124:127], v[84:99]
	ds_read_b128 v[232:235], v246 offset:40960
	s_waitcnt lgkmcnt(11)
	v_mfma_f32_32x32x16_bf16 v[84:99], v[238:241], v[128:131], v[84:99]
	ds_read_b128 v[238:241], v247 offset:40960
	s_waitcnt lgkmcnt(7)
	v_mfma_f32_32x32x16_bf16 v[68:83], v[208:211], v[100:103], v[156:171]
	s_waitcnt lgkmcnt(6)
	v_mfma_f32_32x32x16_bf16 v[68:83], v[212:215], v[104:107], v[68:83]
	s_waitcnt lgkmcnt(5)
	v_mfma_f32_32x32x16_bf16 v[68:83], v[216:219], v[108:111], v[68:83]
	s_waitcnt lgkmcnt(4)
	v_mfma_f32_32x32x16_bf16 v[68:83], v[220:223], v[112:115], v[68:83]
	s_waitcnt lgkmcnt(3)
	v_mfma_f32_32x32x16_bf16 v[68:83], v[224:227], v[116:119], v[68:83]
	s_waitcnt lgkmcnt(2)
	v_mfma_f32_32x32x16_bf16 v[68:83], v[228:231], v[120:123], v[68:83]
	s_waitcnt lgkmcnt(1)
	v_mfma_f32_32x32x16_bf16 v[68:83], v[232:235], v[124:127], v[68:83]
	s_waitcnt lgkmcnt(0)
	v_mfma_f32_32x32x16_bf16 v[68:83], v[238:241], v[128:131], v[68:83]
	ds_read_b64_tr_b16 v[208:209], v174 offset:0
	ds_read_b64_tr_b16 v[210:211], v174 offset:2048
	ds_read_b64_tr_b16 v[212:213], v174 offset:4096
	ds_read_b64_tr_b16 v[214:215], v174 offset:6144
	ds_read_b64_tr_b16 v[216:217], v174 offset:8192
	ds_read_b64_tr_b16 v[218:219], v174 offset:10240
	ds_read_b64_tr_b16 v[220:221], v174 offset:12288
	ds_read_b64_tr_b16 v[222:223], v174 offset:14336
	s_setprio 0
	s_nop 7
	s_nop 3
	v_cmp_eq_f32_e32 vcc, 0, v193
	s_cmp_eq_u64 vcc, exec
	s_cbranch_scc0 .Lsub_a1b0
	v_exp_f32_e32 v140, v84
	v_exp_f32_e32 v141, v85
	v_exp_f32_e32 v142, v86
	v_exp_f32_e32 v143, v87
	v_exp_f32_e32 v144, v88
	v_exp_f32_e32 v145, v89
	v_exp_f32_e32 v146, v90
	v_exp_f32_e32 v147, v91
	v_exp_f32_e32 v148, v92
	v_exp_f32_e32 v149, v93
	v_exp_f32_e32 v150, v94
	v_exp_f32_e32 v151, v95
	v_exp_f32_e32 v152, v96
	v_exp_f32_e32 v153, v97
	v_exp_f32_e32 v154, v98
	v_exp_f32_e32 v155, v99
	v_pk_add_f32 v[250:251], v[140:141], v[142:143]
	v_pk_add_f32 v[250:251], v[250:251], v[144:145]
	v_pk_add_f32 v[250:251], v[250:251], v[146:147]
	v_pk_add_f32 v[250:251], v[250:251], v[148:149]
	v_pk_add_f32 v[250:251], v[250:251], v[150:151]
	v_pk_add_f32 v[250:251], v[250:251], v[152:153]
	v_pk_add_f32 v[250:251], v[250:251], v[154:155]
	v_add_f32_e32 v248, v250, v251
	v_cvt_pk_bf16_f32 v140, v140, v141
	v_cvt_pk_bf16_f32 v141, v142, v143
	v_cvt_pk_bf16_f32 v142, v144, v145
	v_cvt_pk_bf16_f32 v143, v146, v147
	v_cvt_pk_bf16_f32 v144, v148, v149
	v_cvt_pk_bf16_f32 v145, v150, v151
	v_cvt_pk_bf16_f32 v146, v152, v153
	v_cvt_pk_bf16_f32 v147, v154, v155
	s_nop 1
	v_permlane32_swap_b32_e32 v140, v142
	v_permlane32_swap_b32_e32 v141, v143
	v_permlane32_swap_b32_e32 v144, v146
	v_permlane32_swap_b32_e32 v145, v147
	v_exp_f32_e32 v156, v68
	v_exp_f32_e32 v157, v69
	v_exp_f32_e32 v158, v70
	v_exp_f32_e32 v159, v71
	v_exp_f32_e32 v160, v72
	v_exp_f32_e32 v161, v73
	v_exp_f32_e32 v162, v74
	v_exp_f32_e32 v163, v75
	v_exp_f32_e32 v164, v76
	v_exp_f32_e32 v165, v77
	v_exp_f32_e32 v166, v78
	v_exp_f32_e32 v167, v79
	v_exp_f32_e32 v168, v80
	v_exp_f32_e32 v169, v81
	v_exp_f32_e32 v170, v82
	v_exp_f32_e32 v171, v83
	v_pk_add_f32 v[250:251], v[156:157], v[158:159]
	v_pk_add_f32 v[250:251], v[250:251], v[160:161]
	v_pk_add_f32 v[250:251], v[250:251], v[162:163]
	v_pk_add_f32 v[250:251], v[250:251], v[164:165]
	v_pk_add_f32 v[250:251], v[250:251], v[166:167]
	v_pk_add_f32 v[250:251], v[250:251], v[168:169]
	v_pk_add_f32 v[250:251], v[250:251], v[170:171]
	v_add_f32_e32 v249, v250, v251
	v_cvt_pk_bf16_f32 v156, v156, v157
	v_cvt_pk_bf16_f32 v157, v158, v159
	v_cvt_pk_bf16_f32 v158, v160, v161
	v_cvt_pk_bf16_f32 v159, v162, v163
	v_cvt_pk_bf16_f32 v160, v164, v165
	v_cvt_pk_bf16_f32 v161, v166, v167
	v_cvt_pk_bf16_f32 v162, v168, v169
	v_cvt_pk_bf16_f32 v163, v170, v171
	s_nop 1
	v_permlane32_swap_b32_e32 v156, v158
	v_permlane32_swap_b32_e32 v157, v159
	v_permlane32_swap_b32_e32 v160, v162
	v_permlane32_swap_b32_e32 v161, v163
	s_branch .Lsum_a1b0
.Lsub_a1b0:
	v_sub_f32_e32 v140, v84, v193
	v_sub_f32_e32 v141, v85, v193
	v_sub_f32_e32 v142, v86, v193
	v_sub_f32_e32 v143, v87, v193
	v_sub_f32_e32 v144, v88, v193
	v_sub_f32_e32 v145, v89, v193
	v_sub_f32_e32 v146, v90, v193
	v_sub_f32_e32 v147, v91, v193
	v_sub_f32_e32 v148, v92, v193
	v_sub_f32_e32 v149, v93, v193
	v_sub_f32_e32 v150, v94, v193
	v_sub_f32_e32 v151, v95, v193
	v_sub_f32_e32 v152, v96, v193
	v_sub_f32_e32 v153, v97, v193
	v_sub_f32_e32 v154, v98, v193
	v_sub_f32_e32 v155, v99, v193
	v_exp_f32_e32 v140, v140
	v_exp_f32_e32 v141, v141
	v_exp_f32_e32 v142, v142
	v_exp_f32_e32 v143, v143
	v_exp_f32_e32 v144, v144
	v_exp_f32_e32 v145, v145
	v_exp_f32_e32 v146, v146
	v_exp_f32_e32 v147, v147
	v_exp_f32_e32 v148, v148
	v_exp_f32_e32 v149, v149
	v_exp_f32_e32 v150, v150
	v_exp_f32_e32 v151, v151
	v_exp_f32_e32 v152, v152
	v_exp_f32_e32 v153, v153
	v_exp_f32_e32 v154, v154
	v_exp_f32_e32 v155, v155
	v_pk_add_f32 v[250:251], v[140:141], v[142:143]
	v_pk_add_f32 v[250:251], v[250:251], v[144:145]
	v_pk_add_f32 v[250:251], v[250:251], v[146:147]
	v_pk_add_f32 v[250:251], v[250:251], v[148:149]
	v_pk_add_f32 v[250:251], v[250:251], v[150:151]
	v_pk_add_f32 v[250:251], v[250:251], v[152:153]
	v_pk_add_f32 v[250:251], v[250:251], v[154:155]
	v_add_f32_e32 v248, v250, v251
	v_cvt_pk_bf16_f32 v140, v140, v141
	v_cvt_pk_bf16_f32 v141, v142, v143
	v_cvt_pk_bf16_f32 v142, v144, v145
	v_cvt_pk_bf16_f32 v143, v146, v147
	v_cvt_pk_bf16_f32 v144, v148, v149
	v_cvt_pk_bf16_f32 v145, v150, v151
	v_cvt_pk_bf16_f32 v146, v152, v153
	v_cvt_pk_bf16_f32 v147, v154, v155
	s_nop 1
	v_permlane32_swap_b32_e32 v140, v142
	v_permlane32_swap_b32_e32 v141, v143
	v_permlane32_swap_b32_e32 v144, v146
	v_permlane32_swap_b32_e32 v145, v147
	v_sub_f32_e32 v156, v68, v193
	v_sub_f32_e32 v157, v69, v193
	v_sub_f32_e32 v158, v70, v193
	v_sub_f32_e32 v159, v71, v193
	v_sub_f32_e32 v160, v72, v193
	v_sub_f32_e32 v161, v73, v193
	v_sub_f32_e32 v162, v74, v193
	v_sub_f32_e32 v163, v75, v193
	v_sub_f32_e32 v164, v76, v193
	v_sub_f32_e32 v165, v77, v193
	v_sub_f32_e32 v166, v78, v193
	v_sub_f32_e32 v167, v79, v193
	v_sub_f32_e32 v168, v80, v193
	v_sub_f32_e32 v169, v81, v193
	v_sub_f32_e32 v170, v82, v193
	v_sub_f32_e32 v171, v83, v193
	v_exp_f32_e32 v156, v156
	v_exp_f32_e32 v157, v157
	v_exp_f32_e32 v158, v158
	v_exp_f32_e32 v159, v159
	v_exp_f32_e32 v160, v160
	v_exp_f32_e32 v161, v161
	v_exp_f32_e32 v162, v162
	v_exp_f32_e32 v163, v163
	v_exp_f32_e32 v164, v164
	v_exp_f32_e32 v165, v165
	v_exp_f32_e32 v166, v166
	v_exp_f32_e32 v167, v167
	v_exp_f32_e32 v168, v168
	v_exp_f32_e32 v169, v169
	v_exp_f32_e32 v170, v170
	v_exp_f32_e32 v171, v171
	v_pk_add_f32 v[250:251], v[156:157], v[158:159]
	v_pk_add_f32 v[250:251], v[250:251], v[160:161]
	v_pk_add_f32 v[250:251], v[250:251], v[162:163]
	v_pk_add_f32 v[250:251], v[250:251], v[164:165]
	v_pk_add_f32 v[250:251], v[250:251], v[166:167]
	v_pk_add_f32 v[250:251], v[250:251], v[168:169]
	v_pk_add_f32 v[250:251], v[250:251], v[170:171]
	v_add_f32_e32 v249, v250, v251
	v_cvt_pk_bf16_f32 v156, v156, v157
	v_cvt_pk_bf16_f32 v157, v158, v159
	v_cvt_pk_bf16_f32 v158, v160, v161
	v_cvt_pk_bf16_f32 v159, v162, v163
	v_cvt_pk_bf16_f32 v160, v164, v165
	v_cvt_pk_bf16_f32 v161, v166, v167
	v_cvt_pk_bf16_f32 v162, v168, v169
	v_cvt_pk_bf16_f32 v163, v170, v171
	s_nop 1
	v_permlane32_swap_b32_e32 v156, v158
	v_permlane32_swap_b32_e32 v157, v159
	v_permlane32_swap_b32_e32 v160, v162
	v_permlane32_swap_b32_e32 v161, v163

.LBB0_1467:
	s_add_i32 s98, s18, 64
	s_cmp_le_i32 s98, s40
	s_cbranch_scc0 .Lorig_a1b1
	s_setprio 3
	ds_read_b128 v[140:143], v177
	ds_read_b128 v[144:147], v177 offset:32
	ds_read_b128 v[148:151], v177 offset:64
	ds_read_b128 v[152:155], v177 offset:96
	ds_read_b128 v[208:211], v172 offset:49152
	ds_read_b128 v[212:215], v206 offset:49152
	ds_read_b128 v[216:219], v207 offset:49152
	ds_read_b128 v[220:223], v237 offset:49152
	ds_read_b128 v[224:227], v244 offset:49152
	ds_read_b128 v[228:231], v245 offset:49152
	ds_read_b128 v[232:235], v246 offset:49152
	ds_read_b128 v[238:241], v247 offset:49152
	ds_read_b128 v[156:159], v177 offset:128
	ds_read_b128 v[160:163], v177 offset:160
	ds_read_b128 v[164:167], v177 offset:192
	ds_read_b128 v[168:171], v177 offset:224
	s_waitcnt lgkmcnt(11)
	v_mfma_f32_32x32x16_bf16 v[84:99], v[208:211], v[100:103], v[140:155]
	ds_read_b128 v[208:211], v172 offset:57344
	s_waitcnt lgkmcnt(11)
	v_mfma_f32_32x32x16_bf16 v[84:99], v[212:215], v[104:107], v[84:99]
	ds_read_b128 v[212:215], v206 offset:57344
	s_waitcnt lgkmcnt(11)
	v_mfma_f32_32x32x16_bf16 v[84:99], v[216:219], v[108:111], v[84:99]
	ds_read_b128 v[216:219], v207 offset:57344
	s_waitcnt lgkmcnt(11)
	v_mfma_f32_32x32x16_bf16 v[84:99], v[220:223], v[112:115], v[84:99]
	ds_read_b128 v[220:223], v237 offset:57344
	s_waitcnt lgkmcnt(11)
	v_mfma_f32_32x32x16_bf16 v[84:99], v[224:227], v[116:119], v[84:99]
	ds_read_b128 v[224:227], v244 offset:57344
	s_waitcnt lgkmcnt(11)
	v_mfma_f32_32x32x16_bf16 v[84:99], v[228:231], v[120:123], v[84:99]
	ds_read_b128 v[228:231], v245 offset:57344
	s_waitcnt lgkmcnt(11)
	v_mfma_f32_32x32x16_bf16 v[84:99], v[232:235], v[124:127], v[84:99]
	ds_read_b128 v[232:235], v246 offset:57344
	s_waitcnt lgkmcnt(11)
	v_mfma_f32_32x32x16_bf16 v[84:99], v[238:241], v[128:131], v[84:99]
	ds_read_b128 v[238:241], v247 offset:57344
	s_waitcnt lgkmcnt(7)
	v_mfma_f32_32x32x16_bf16 v[68:83], v[208:211], v[100:103], v[156:171]
	s_waitcnt lgkmcnt(6)
	v_mfma_f32_32x32x16_bf16 v[68:83], v[212:215], v[104:107], v[68:83]
	s_waitcnt lgkmcnt(5)
	v_mfma_f32_32x32x16_bf16 v[68:83], v[216:219], v[108:111], v[68:83]
	s_waitcnt lgkmcnt(4)
	v_mfma_f32_32x32x16_bf16 v[68:83], v[220:223], v[112:115], v[68:83]
	s_waitcnt lgkmcnt(3)
	v_mfma_f32_32x32x16_bf16 v[68:83], v[224:227], v[116:119], v[68:83]
	s_waitcnt lgkmcnt(2)
	v_mfma_f32_32x32x16_bf16 v[68:83], v[228:231], v[120:123], v[68:83]
	s_waitcnt lgkmcnt(1)
	v_mfma_f32_32x32x16_bf16 v[68:83], v[232:235], v[124:127], v[68:83]
	s_waitcnt lgkmcnt(0)
	v_mfma_f32_32x32x16_bf16 v[68:83], v[238:241], v[128:131], v[68:83]
	ds_read_b64_tr_b16 v[208:209], v174 offset:16384
	ds_read_b64_tr_b16 v[210:211], v174 offset:18432
	ds_read_b64_tr_b16 v[212:213], v174 offset:20480
	ds_read_b64_tr_b16 v[214:215], v174 offset:22528
	ds_read_b64_tr_b16 v[216:217], v174 offset:24576
	ds_read_b64_tr_b16 v[218:219], v174 offset:26624
	ds_read_b64_tr_b16 v[220:221], v174 offset:28672
	ds_read_b64_tr_b16 v[222:223], v174 offset:30720
	s_setprio 0
	s_nop 7
	s_nop 3
	v_cmp_eq_f32_e32 vcc, 0, v192
	s_cmp_eq_u64 vcc, exec
	s_cbranch_scc0 .Lsub_a1b1
	v_exp_f32_e32 v140, v84
	v_exp_f32_e32 v141, v85
	v_exp_f32_e32 v142, v86
	v_exp_f32_e32 v143, v87
	v_exp_f32_e32 v144, v88
	v_exp_f32_e32 v145, v89
	v_exp_f32_e32 v146, v90
	v_exp_f32_e32 v147, v91
	v_exp_f32_e32 v148, v92
	v_exp_f32_e32 v149, v93
	v_exp_f32_e32 v150, v94
	v_exp_f32_e32 v151, v95
	v_exp_f32_e32 v152, v96
	v_exp_f32_e32 v153, v97
	v_exp_f32_e32 v154, v98
	v_exp_f32_e32 v155, v99
	v_pk_add_f32 v[250:251], v[140:141], v[142:143]
	v_pk_add_f32 v[250:251], v[250:251], v[144:145]
	v_pk_add_f32 v[250:251], v[250:251], v[146:147]
	v_pk_add_f32 v[250:251], v[250:251], v[148:149]
	v_pk_add_f32 v[250:251], v[250:251], v[150:151]
	v_pk_add_f32 v[250:251], v[250:251], v[152:153]
	v_pk_add_f32 v[250:251], v[250:251], v[154:155]
	v_add_f32_e32 v248, v250, v251
	v_cvt_pk_bf16_f32 v140, v140, v141
	v_cvt_pk_bf16_f32 v141, v142, v143
	v_cvt_pk_bf16_f32 v142, v144, v145
	v_cvt_pk_bf16_f32 v143, v146, v147
	v_cvt_pk_bf16_f32 v144, v148, v149
	v_cvt_pk_bf16_f32 v145, v150, v151
	v_cvt_pk_bf16_f32 v146, v152, v153
	v_cvt_pk_bf16_f32 v147, v154, v155
	s_nop 1
	v_permlane32_swap_b32_e32 v140, v142
	v_permlane32_swap_b32_e32 v141, v143
	v_permlane32_swap_b32_e32 v144, v146
	v_permlane32_swap_b32_e32 v145, v147
	v_exp_f32_e32 v156, v68
	v_exp_f32_e32 v157, v69
	v_exp_f32_e32 v158, v70
	v_exp_f32_e32 v159, v71
	v_exp_f32_e32 v160, v72
	v_exp_f32_e32 v161, v73
	v_exp_f32_e32 v162, v74
	v_exp_f32_e32 v163, v75
	v_exp_f32_e32 v164, v76
	v_exp_f32_e32 v165, v77
	v_exp_f32_e32 v166, v78
	v_exp_f32_e32 v167, v79
	v_exp_f32_e32 v168, v80
	v_exp_f32_e32 v169, v81
	v_exp_f32_e32 v170, v82
	v_exp_f32_e32 v171, v83
	v_pk_add_f32 v[250:251], v[156:157], v[158:159]
	v_pk_add_f32 v[250:251], v[250:251], v[160:161]
	v_pk_add_f32 v[250:251], v[250:251], v[162:163]
	v_pk_add_f32 v[250:251], v[250:251], v[164:165]
	v_pk_add_f32 v[250:251], v[250:251], v[166:167]
	v_pk_add_f32 v[250:251], v[250:251], v[168:169]
	v_pk_add_f32 v[250:251], v[250:251], v[170:171]
	v_add_f32_e32 v249, v250, v251
	v_cvt_pk_bf16_f32 v156, v156, v157
	v_cvt_pk_bf16_f32 v157, v158, v159
	v_cvt_pk_bf16_f32 v158, v160, v161
	v_cvt_pk_bf16_f32 v159, v162, v163
	v_cvt_pk_bf16_f32 v160, v164, v165
	v_cvt_pk_bf16_f32 v161, v166, v167
	v_cvt_pk_bf16_f32 v162, v168, v169
	v_cvt_pk_bf16_f32 v163, v170, v171
	s_nop 1
	v_permlane32_swap_b32_e32 v156, v158
	v_permlane32_swap_b32_e32 v157, v159
	v_permlane32_swap_b32_e32 v160, v162
	v_permlane32_swap_b32_e32 v161, v163
	s_branch .Lsum_a1b1
.Lsub_a1b1:
	v_sub_f32_e32 v140, v84, v192
	v_sub_f32_e32 v141, v85, v192
	v_sub_f32_e32 v142, v86, v192
	v_sub_f32_e32 v143, v87, v192
	v_sub_f32_e32 v144, v88, v192
	v_sub_f32_e32 v145, v89, v192
	v_sub_f32_e32 v146, v90, v192
	v_sub_f32_e32 v147, v91, v192
	v_sub_f32_e32 v148, v92, v192
	v_sub_f32_e32 v149, v93, v192
	v_sub_f32_e32 v150, v94, v192
	v_sub_f32_e32 v151, v95, v192
	v_sub_f32_e32 v152, v96, v192
	v_sub_f32_e32 v153, v97, v192
	v_sub_f32_e32 v154, v98, v192
	v_sub_f32_e32 v155, v99, v192
	v_exp_f32_e32 v140, v140
	v_exp_f32_e32 v141, v141
	v_exp_f32_e32 v142, v142
	v_exp_f32_e32 v143, v143
	v_exp_f32_e32 v144, v144
	v_exp_f32_e32 v145, v145
	v_exp_f32_e32 v146, v146
	v_exp_f32_e32 v147, v147
	v_exp_f32_e32 v148, v148
	v_exp_f32_e32 v149, v149
	v_exp_f32_e32 v150, v150
	v_exp_f32_e32 v151, v151
	v_exp_f32_e32 v152, v152
	v_exp_f32_e32 v153, v153
	v_exp_f32_e32 v154, v154
	v_exp_f32_e32 v155, v155
	v_pk_add_f32 v[250:251], v[140:141], v[142:143]
	v_pk_add_f32 v[250:251], v[250:251], v[144:145]
	v_pk_add_f32 v[250:251], v[250:251], v[146:147]
	v_pk_add_f32 v[250:251], v[250:251], v[148:149]
	v_pk_add_f32 v[250:251], v[250:251], v[150:151]
	v_pk_add_f32 v[250:251], v[250:251], v[152:153]
	v_pk_add_f32 v[250:251], v[250:251], v[154:155]
	v_add_f32_e32 v248, v250, v251
	v_cvt_pk_bf16_f32 v140, v140, v141
	v_cvt_pk_bf16_f32 v141, v142, v143
	v_cvt_pk_bf16_f32 v142, v144, v145
	v_cvt_pk_bf16_f32 v143, v146, v147
	v_cvt_pk_bf16_f32 v144, v148, v149
	v_cvt_pk_bf16_f32 v145, v150, v151
	v_cvt_pk_bf16_f32 v146, v152, v153
	v_cvt_pk_bf16_f32 v147, v154, v155
	s_nop 1
	v_permlane32_swap_b32_e32 v140, v142
	v_permlane32_swap_b32_e32 v141, v143
	v_permlane32_swap_b32_e32 v144, v146
	v_permlane32_swap_b32_e32 v145, v147
	v_sub_f32_e32 v156, v68, v192
	v_sub_f32_e32 v157, v69, v192
	v_sub_f32_e32 v158, v70, v192
	v_sub_f32_e32 v159, v71, v192
	v_sub_f32_e32 v160, v72, v192
	v_sub_f32_e32 v161, v73, v192
	v_sub_f32_e32 v162, v74, v192
	v_sub_f32_e32 v163, v75, v192
	v_sub_f32_e32 v164, v76, v192
	v_sub_f32_e32 v165, v77, v192
	v_sub_f32_e32 v166, v78, v192
	v_sub_f32_e32 v167, v79, v192
	v_sub_f32_e32 v168, v80, v192
	v_sub_f32_e32 v169, v81, v192
	v_sub_f32_e32 v170, v82, v192
	v_sub_f32_e32 v171, v83, v192
	v_exp_f32_e32 v156, v156
	v_exp_f32_e32 v157, v157
	v_exp_f32_e32 v158, v158
	v_exp_f32_e32 v159, v159
	v_exp_f32_e32 v160, v160
	v_exp_f32_e32 v161, v161
	v_exp_f32_e32 v162, v162
	v_exp_f32_e32 v163, v163
	v_exp_f32_e32 v164, v164
	v_exp_f32_e32 v165, v165
	v_exp_f32_e32 v166, v166
	v_exp_f32_e32 v167, v167
	v_exp_f32_e32 v168, v168
	v_exp_f32_e32 v169, v169
	v_exp_f32_e32 v170, v170
	v_exp_f32_e32 v171, v171
	v_pk_add_f32 v[250:251], v[156:157], v[158:159]
	v_pk_add_f32 v[250:251], v[250:251], v[160:161]
	v_pk_add_f32 v[250:251], v[250:251], v[162:163]
	v_pk_add_f32 v[250:251], v[250:251], v[164:165]
	v_pk_add_f32 v[250:251], v[250:251], v[166:167]
	v_pk_add_f32 v[250:251], v[250:251], v[168:169]
	v_pk_add_f32 v[250:251], v[250:251], v[170:171]
	v_add_f32_e32 v249, v250, v251
	v_cvt_pk_bf16_f32 v156, v156, v157
	v_cvt_pk_bf16_f32 v157, v158, v159
	v_cvt_pk_bf16_f32 v158, v160, v161
	v_cvt_pk_bf16_f32 v159, v162, v163
	v_cvt_pk_bf16_f32 v160, v164, v165
	v_cvt_pk_bf16_f32 v161, v166, v167
	v_cvt_pk_bf16_f32 v162, v168, v169
	v_cvt_pk_bf16_f32 v163, v170, v171
	s_nop 1
	v_permlane32_swap_b32_e32 v156, v158
	v_permlane32_swap_b32_e32 v157, v159
	v_permlane32_swap_b32_e32 v160, v162
	v_permlane32_swap_b32_e32 v161, v163
